# speedup vs baseline: 1.0038x; 1.0038x over previous
.LBB1_3:
	s_mov_b32 s29, s16
	v_add_u32_e32 v0, s29, v101
	ds_read_b128 v[94:97], v0 offset:16384
	ds_read_b128 v[102:105], v0 offset:17408
	ds_read_b128 v[106:109], v0 offset:18432
	ds_read_b128 v[110:113], v0 offset:19456
	ds_read_b128 v[114:117], v0 offset:32768
	ds_read_b128 v[118:121], v0 offset:33792
	ds_read_b128 v[122:125], v0 offset:34816
	ds_read_b128 v[126:129], v0 offset:35840
	s_lshl_b32 s16, s28, 2
	s_or_b32 s16, s16, s23
	s_lshl_b64 s[30:31], s[16:17], 19
	s_add_u32 s16, s6, s30
	s_addc_u32 s31, s7, s31
	s_lshl_b32 s33, s3, 7
	s_ashr_i32 s35, s33, 31
	s_add_u32 s30, s16, s33
	s_addc_u32 s31, s31, s35
	s_add_u32 s34, s4, s33
	s_addc_u32 s35, s5, s35
	s_add_i32 s16, s19, s27
	s_add_i32 m0, s16, 0x4000
	v_add_u32_e32 v0, s29, v91
	global_load_lds_dwordx4 v84, s[30:31]
	ds_read_b128 v[130:133], v0
	ds_read_b128 v[134:137], v0 offset:1024
	s_add_i32 m0, s16, 0x6000
	ds_read_b128 v[138:141], v0 offset:2048
	global_load_lds_dwordx4 v88, s[30:31]
	ds_read_b128 v[142:145], v0 offset:3072
	ds_read_b128 v[146:149], v0 offset:4096
	s_mov_b32 m0, s16
	ds_read_b128 v[150:153], v0 offset:5120
	global_load_lds_dwordx4 v82, s[34:35]
	ds_read_b128 v[154:157], v0 offset:6144
	ds_read_b128 v[158:161], v0 offset:7168
	s_waitcnt vmcnt(3)
	s_waitcnt lgkmcnt(0)
	s_barrier
	s_setprio 1
	s_waitcnt lgkmcnt(0)
	v_mfma_f32_16x16x32_f16 v[78:81], v[94:97], v[130:133], v[78:81]
	s_add_u32 s30, s30, 0x40000
	s_addc_u32 s31, s31, 0
	s_add_i32 m0, s16, 0x8000
	v_mfma_f32_16x16x32_f16 v[74:77], v[106:109], v[130:133], v[74:77]
	global_load_lds_dwordx4 v84, s[30:31]
	s_add_i32 m0, s16, 0xa000
	v_mfma_f32_16x16x32_f16 v[66:69], v[94:97], v[138:141], v[66:69]
	global_load_lds_dwordx4 v88, s[30:31]
	s_add_i32 m0, s16, 0x2000
	v_mfma_f32_16x16x32_f16 v[58:61], v[106:109], v[138:141], v[58:61]
	global_load_lds_dwordx4 v86, s[34:35]
	v_mfma_f32_16x16x32_f16 v[78:81], v[102:105], v[134:137], v[78:81]
	v_mfma_f32_16x16x32_f16 v[74:77], v[110:113], v[134:137], v[74:77]
	v_mfma_f32_16x16x32_f16 v[66:69], v[102:105], v[142:145], v[66:69]
	v_mfma_f32_16x16x32_f16 v[58:61], v[110:113], v[142:145], v[58:61]
	v_mfma_f32_16x16x32_f16 v[54:57], v[94:97], v[146:149], v[54:57]
	v_mfma_f32_16x16x32_f16 v[46:49], v[106:109], v[146:149], v[46:49]
	v_mfma_f32_16x16x32_f16 v[34:37], v[94:97], v[154:157], v[34:37]
	v_mfma_f32_16x16x32_f16 v[26:29], v[106:109], v[154:157], v[26:29]
	v_mfma_f32_16x16x32_f16 v[54:57], v[102:105], v[150:153], v[54:57]
	v_mfma_f32_16x16x32_f16 v[46:49], v[110:113], v[150:153], v[46:49]
	v_mfma_f32_16x16x32_f16 v[34:37], v[102:105], v[158:161], v[34:37]
	v_mfma_f32_16x16x32_f16 v[26:29], v[110:113], v[158:161], v[26:29]
	v_mfma_f32_16x16x32_f16 v[70:73], v[114:117], v[130:133], v[70:73]
	v_mfma_f32_16x16x32_f16 v[62:65], v[122:125], v[130:133], v[62:65]
	v_mfma_f32_16x16x32_f16 v[50:53], v[114:117], v[138:141], v[50:53]
	v_mfma_f32_16x16x32_f16 v[42:45], v[122:125], v[138:141], v[42:45]
	v_mfma_f32_16x16x32_f16 v[70:73], v[118:121], v[134:137], v[70:73]
	v_mfma_f32_16x16x32_f16 v[62:65], v[126:129], v[134:137], v[62:65]
	v_mfma_f32_16x16x32_f16 v[50:53], v[118:121], v[142:145], v[50:53]
	v_mfma_f32_16x16x32_f16 v[42:45], v[126:129], v[142:145], v[42:45]
	v_mfma_f32_16x16x32_f16 v[38:41], v[114:117], v[146:149], v[38:41]
	v_mfma_f32_16x16x32_f16 v[30:33], v[122:125], v[146:149], v[30:33]
	s_add_i32 s3, s3, 1
	s_bitcmp1_b32 s3, 4
	s_addc_u32 s28, s28, 0
	v_mfma_f32_16x16x32_f16 v[22:25], v[114:117], v[154:157], v[22:25]
	s_and_b32 s3, s3, 15
	v_mfma_f32_16x16x32_f16 v[2:5], v[122:125], v[154:157], v[2:5]
	v_mfma_f32_16x16x32_f16 v[38:41], v[118:121], v[150:153], v[38:41]
	v_mfma_f32_16x16x32_f16 v[30:33], v[126:129], v[150:153], v[30:33]
	s_add_i32 s26, s26, -1
	v_mfma_f32_16x16x32_f16 v[22:25], v[118:121], v[158:161], v[22:25]
	s_mov_b32 s16, s24
	s_mov_b32 s24, s27
	v_mfma_f32_16x16x32_f16 v[2:5], v[126:129], v[158:161], v[2:5]
	s_mov_b32 s27, s29
	s_cmp_lg_u32 s26, 0
	s_setprio 0
	s_barrier
	s_cbranch_scc1 .LBB1_3
	s_lshl_b32 s3, s14, 7
	s_add_i32 s17, s25, s3
	s_ashr_i32 s3, s17, 1
	s_lshr_b32 s14, s17, 5
	s_or_b32 s24, s15, s2
	s_and_b32 s14, s14, 62
	s_and_b32 s27, s3, 0xfffffc00
	v_or_b32_e32 v105, s24, v1
	v_lshlrev_b32_e32 v98, 4, v93
	v_or_b32_e32 v102, 16, v93
	v_or_b32_e32 v103, 32, v93
	v_or_b32_e32 v104, 48, v93
	v_mov_b32_e32 v93, 0
	s_and_b32 s16, s24, 0x340
	v_lshlrev_b32_e32 v95, 6, v105
	s_or_b32 s2, s27, s14
	v_lshlrev_b32_e32 v0, 9, v92
	v_and_b32_e32 v110, 0xc00, v95
	v_mov_b32_e32 v111, v93
	s_or_b32 s14, s2, s16
	v_and_b32_e32 v92, 0x200, v0
	v_lshl_add_u64 v[110:111], s[8:9], 0, v[110:111]
	s_or_b32 s30, s14, 0x80
	s_mov_b32 s3, 0
	v_mov_b32_e32 v99, v93
	v_lshl_add_u64 v[110:111], v[110:111], 0, v[92:93]
	s_mov_b32 s2, 0x3e38aa3b
	v_pk_add_f32 v[72:73], v[12:13], v[72:73]
	v_pk_add_f32 v[70:71], v[10:11], v[70:71]
	v_pk_add_f32 v[64:65], v[8:9], v[64:65]
	v_pk_add_f32 v[62:63], v[6:7], v[62:63]
	s_ashr_i32 s31, s30, 31
	v_lshl_add_u64 v[112:113], v[110:111], 0, v[98:99]
	v_pk_mul_f32 v[72:73], v[72:73], s[2:3] op_sel_hi:[1,0]
	v_pk_mul_f32 v[70:71], v[70:71], s[2:3] op_sel_hi:[1,0]
	v_pk_mul_f32 v[64:65], v[64:65], s[2:3] op_sel_hi:[1,0]
	v_pk_mul_f32 v[62:63], v[62:63], s[2:3] op_sel_hi:[1,0]
	s_lshl_b64 s[30:31], s[30:31], 12
	v_lshlrev_b32_e32 v96, 4, v102
	v_mov_b32_e32 v97, v93
	v_pk_add_f32 v[80:81], v[20:21], v[80:81]
	v_pk_add_f32 v[78:79], v[18:19], v[78:79]
	v_pk_add_f32 v[74:75], v[14:15], v[74:75]
	s_ashr_i32 s15, s14, 31
	v_cvt_pk_f16_f32 v70, v70, v71
	v_cvt_pk_f16_f32 v71, v72, v73
	v_cvt_pk_f16_f32 v72, v62, v63
	v_cvt_pk_f16_f32 v73, v64, v65
	v_lshl_add_u64 v[62:63], v[112:113], 0, s[30:31]
	v_pk_add_f32 v[58:59], v[14:15], v[58:59]
	v_pk_mul_f32 v[80:81], v[80:81], s[2:3] op_sel_hi:[1,0]
	v_pk_mul_f32 v[78:79], v[78:79], s[2:3] op_sel_hi:[1,0]
	v_pk_mul_f32 v[74:75], v[74:75], s[2:3] op_sel_hi:[1,0]
	s_lshl_b64 s[28:29], s[14:15], 12
	global_store_dwordx4 v[62:63], v[70:73], off
	v_pk_add_f32 v[62:63], v[20:21], v[68:69]
	v_pk_add_f32 v[64:65], v[18:19], v[66:67]
	v_lshl_add_u64 v[70:71], v[110:111], 0, v[96:97]
	v_pk_mul_f32 v[58:59], v[58:59], s[2:3] op_sel_hi:[1,0]
	v_pk_add_f32 v[52:53], v[12:13], v[52:53]
	v_pk_add_f32 v[50:51], v[10:11], v[50:51]
	v_pk_add_f32 v[44:45], v[8:9], v[44:45]
	v_pk_add_f32 v[42:43], v[6:7], v[42:43]
	v_lshlrev_b32_e32 v0, 4, v103
	v_cvt_pk_f16_f32 v78, v78, v79
	v_cvt_pk_f16_f32 v79, v80, v81
	v_cvt_pk_f16_f32 v80, v74, v75
	v_lshl_add_u64 v[74:75], v[112:113], 0, s[28:29]
	v_pk_mul_f32 v[66:67], v[62:63], s[2:3] op_sel_hi:[1,0]
	v_pk_mul_f32 v[62:63], v[64:65], s[2:3] op_sel_hi:[1,0]
	v_cvt_pk_f16_f32 v64, v58, v59
	v_lshl_add_u64 v[58:59], v[70:71], 0, s[28:29]
	v_pk_mul_f32 v[52:53], v[52:53], s[2:3] op_sel_hi:[1,0]
	v_pk_mul_f32 v[50:51], v[50:51], s[2:3] op_sel_hi:[1,0]
	v_pk_mul_f32 v[44:45], v[44:45], s[2:3] op_sel_hi:[1,0]
	v_pk_mul_f32 v[42:43], v[42:43], s[2:3] op_sel_hi:[1,0]
	s_or_b32 s28, s14, 1
	s_or_b32 s14, s14, 0x81
	v_and_b32_e32 v106, 0xf0, v0
	v_mov_b32_e32 v107, v93
	v_cvt_pk_f16_f32 v50, v50, v51
	v_cvt_pk_f16_f32 v51, v52, v53
	v_cvt_pk_f16_f32 v52, v42, v43
	v_cvt_pk_f16_f32 v53, v44, v45
	v_lshl_add_u64 v[42:43], v[70:71], 0, s[30:31]
	v_pk_add_f32 v[40:41], v[12:13], v[40:41]
	v_pk_add_f32 v[38:39], v[10:11], v[38:39]
	v_pk_add_f32 v[32:33], v[8:9], v[32:33]
	v_pk_add_f32 v[30:31], v[6:7], v[30:31]
	s_ashr_i32 s15, s14, 31
	v_lshlrev_b32_e32 v94, 4, v104
	global_store_dwordx4 v[42:43], v[50:53], off
	v_pk_mul_f32 v[40:41], v[40:41], s[2:3] op_sel_hi:[1,0]
	v_pk_mul_f32 v[38:39], v[38:39], s[2:3] op_sel_hi:[1,0]
	v_lshl_add_u64 v[50:51], v[110:111], 0, v[106:107]
	v_pk_mul_f32 v[32:33], v[32:33], s[2:3] op_sel_hi:[1,0]
	v_pk_mul_f32 v[30:31], v[30:31], s[2:3] op_sel_hi:[1,0]
	s_lshl_b64 s[14:15], s[14:15], 12
	v_and_b32_e32 v108, 0x1f0, v94
	v_mov_b32_e32 v109, v93
	v_pk_add_f32 v[42:43], v[20:21], v[56:57]
	v_pk_add_f32 v[44:45], v[18:19], v[54:55]
	v_pk_add_f32 v[46:47], v[14:15], v[46:47]
	s_ashr_i32 s29, s28, 31
	v_cvt_pk_f16_f32 v38, v38, v39
	v_cvt_pk_f16_f32 v39, v40, v41
	v_cvt_pk_f16_f32 v40, v30, v31
	v_cvt_pk_f16_f32 v41, v32, v33
	v_lshl_add_u64 v[30:31], v[50:51], 0, s[14:15]
	v_pk_add_f32 v[20:21], v[20:21], v[36:37]
	v_pk_add_f32 v[18:19], v[18:19], v[34:35]
	v_pk_add_f32 v[14:15], v[14:15], v[26:27]
	v_pk_add_f32 v[76:77], v[16:17], v[76:77]
	v_pk_add_f32 v[60:61], v[16:17], v[60:61]
	v_pk_mul_f32 v[52:53], v[42:43], s[2:3] op_sel_hi:[1,0]
	v_pk_mul_f32 v[42:43], v[44:45], s[2:3] op_sel_hi:[1,0]
	v_pk_add_f32 v[44:45], v[16:17], v[48:49]
	s_lshl_b64 s[28:29], s[28:29], 12
	global_store_dwordx4 v[30:31], v[38:41], off
	v_lshl_add_u64 v[30:31], v[110:111], 0, v[108:109]
	v_pk_mul_f32 v[20:21], v[20:21], s[2:3] op_sel_hi:[1,0]
	v_pk_mul_f32 v[18:19], v[18:19], s[2:3] op_sel_hi:[1,0]
	v_pk_add_f32 v[16:17], v[16:17], v[28:29]
	v_pk_mul_f32 v[14:15], v[14:15], s[2:3] op_sel_hi:[1,0]
	v_pk_add_f32 v[12:13], v[12:13], v[24:25]
	v_pk_add_f32 v[10:11], v[10:11], v[22:23]
	v_pk_add_f32 v[4:5], v[8:9], v[4:5]
	v_pk_add_f32 v[2:3], v[6:7], v[2:3]
	v_pk_mul_f32 v[76:77], v[76:77], s[2:3] op_sel_hi:[1,0]
	v_pk_mul_f32 v[60:61], v[60:61], s[2:3] op_sel_hi:[1,0]
	v_pk_mul_f32 v[48:49], v[44:45], s[2:3] op_sel_hi:[1,0]
	v_pk_mul_f32 v[44:45], v[46:47], s[2:3] op_sel_hi:[1,0]
	v_lshl_add_u64 v[46:47], v[50:51], 0, s[28:29]
	v_cvt_pk_f16_f32 v18, v18, v19
	v_cvt_pk_f16_f32 v19, v20, v21
	v_pk_mul_f32 v[16:17], v[16:17], s[2:3] op_sel_hi:[1,0]
	v_cvt_pk_f16_f32 v20, v14, v15
	v_lshl_add_u64 v[14:15], v[30:31], 0, s[28:29]
	v_pk_mul_f32 v[12:13], v[12:13], s[2:3] op_sel_hi:[1,0]
	v_pk_mul_f32 v[10:11], v[10:11], s[2:3] op_sel_hi:[1,0]
	v_pk_mul_f32 v[4:5], v[4:5], s[2:3] op_sel_hi:[1,0]
	v_pk_mul_f32 v[2:3], v[2:3], s[2:3] op_sel_hi:[1,0]
	s_add_u32 s28, s20, s22
	v_cvt_pk_f16_f32 v81, v76, v77
	v_cvt_pk_f16_f32 v62, v62, v63
	v_cvt_pk_f16_f32 v63, v66, v67
	v_cvt_pk_f16_f32 v65, v60, v61
	v_cvt_pk_f16_f32 v42, v42, v43
	v_cvt_pk_f16_f32 v43, v52, v53
	v_cvt_pk_f16_f32 v44, v44, v45
	v_cvt_pk_f16_f32 v45, v48, v49
	v_cvt_pk_f16_f32 v21, v16, v17
	v_cvt_pk_f16_f32 v10, v10, v11
	v_cvt_pk_f16_f32 v11, v12, v13
	v_cvt_pk_f16_f32 v12, v2, v3
	v_cvt_pk_f16_f32 v13, v4, v5
	v_lshl_add_u64 v[2:3], v[30:31], 0, s[14:15]
	s_addc_u32 s29, s21, 0
	v_lshlrev_b32_e32 v92, 2, v1
	global_store_dwordx4 v[74:75], v[78:81], off
	global_store_dwordx4 v[58:59], v[62:65], off
	global_store_dwordx4 v[46:47], v[42:45], off
	global_store_dwordx4 v[14:15], v[18:21], off
	global_store_dwordx4 v[2:3], v[10:13], off
	v_lshl_add_u64 v[2:3], s[28:29], 0, v[92:93]
	s_mov_b64 s[28:29], 0x1000
	v_lshl_add_u64 v[10:11], v[2:3], 0, s[28:29]
	global_load_dwordx4 v[22:25], v[10:11], off
	global_load_dwordx4 v[14:17], v[10:11], off offset:16
	global_load_dwordx4 v[6:9], v[10:11], off offset:512
	global_load_dwordx4 v[2:5], v[10:11], off offset:528
	s_mov_b32 s25, 1
	s_mov_b32 s26, 16
	s_mov_b32 s14, 2
	s_mov_b32 s15, 0x18000
	s_mov_b32 s2, 0xc000
	s_mov_b32 s27, 0
	v_mov_b32_e32 v10, v93
	v_mov_b32_e32 v11, v93
	v_mov_b32_e32 v12, v93
	v_mov_b32_e32 v13, v93
	v_mov_b32_e32 v18, v93
	v_mov_b32_e32 v19, v93
	v_mov_b32_e32 v20, v93
	v_mov_b32_e32 v21, v93
	v_mov_b32_e32 v26, v93
	v_mov_b32_e32 v27, v93
	v_mov_b32_e32 v28, v93
	v_mov_b32_e32 v29, v93
	v_mov_b32_e32 v34, v93
	v_mov_b32_e32 v35, v93
	v_mov_b32_e32 v36, v93
	v_mov_b32_e32 v37, v93
	v_mov_b32_e32 v42, v93
	v_mov_b32_e32 v43, v93
	v_mov_b32_e32 v44, v93
	v_mov_b32_e32 v45, v93
	v_mov_b32_e32 v50, v93
	v_mov_b32_e32 v51, v93
	v_mov_b32_e32 v52, v93
	v_mov_b32_e32 v53, v93
	v_mov_b32_e32 v62, v93
	v_mov_b32_e32 v63, v93
	v_mov_b32_e32 v64, v93
	v_mov_b32_e32 v65, v93
	v_mov_b32_e32 v70, v93
	v_mov_b32_e32 v71, v93
	v_mov_b32_e32 v72, v93
	v_mov_b32_e32 v73, v93
	v_mov_b32_e32 v30, v93
	v_mov_b32_e32 v31, v93
	v_mov_b32_e32 v32, v93
	v_mov_b32_e32 v33, v93
	v_mov_b32_e32 v38, v93
	v_mov_b32_e32 v39, v93
	v_mov_b32_e32 v40, v93
	v_mov_b32_e32 v41, v93
	v_mov_b32_e32 v46, v93
	v_mov_b32_e32 v47, v93
	v_mov_b32_e32 v48, v93
	v_mov_b32_e32 v49, v93
	v_mov_b32_e32 v54, v93
	v_mov_b32_e32 v55, v93
	v_mov_b32_e32 v56, v93
	v_mov_b32_e32 v57, v93
	v_mov_b32_e32 v58, v93
	v_mov_b32_e32 v59, v93
	v_mov_b32_e32 v60, v93
	v_mov_b32_e32 v61, v93
	v_mov_b32_e32 v66, v93
	v_mov_b32_e32 v67, v93
	v_mov_b32_e32 v68, v93
	v_mov_b32_e32 v69, v93
	v_mov_b32_e32 v74, v93
	v_mov_b32_e32 v75, v93
	v_mov_b32_e32 v76, v93
	v_mov_b32_e32 v77, v93
	v_mov_b32_e32 v78, v93
	v_mov_b32_e32 v79, v93
	v_mov_b32_e32 v80, v93
	v_mov_b32_e32 v81, v93
.LBB1_5:
	s_mov_b32 s28, s2
	v_add_u32_e32 v1, s28, v101
	ds_read_b128 v[106:109], v1 offset:16384
	ds_read_b128 v[110:113], v1 offset:17408
	ds_read_b128 v[114:117], v1 offset:18432
	ds_read_b128 v[118:121], v1 offset:19456
	ds_read_b128 v[122:125], v1 offset:32768
	ds_read_b128 v[126:129], v1 offset:33792
	ds_read_b128 v[130:133], v1 offset:34816
	ds_read_b128 v[134:137], v1 offset:35840
	s_lshl_b32 s2, s25, 2
	s_or_b32 s2, s2, s23
	s_lshl_b64 s[30:31], s[2:3], 19
	s_add_u32 s2, s6, s30
	s_addc_u32 s29, s7, s31
	s_lshl_b32 s33, s14, 7
	s_ashr_i32 s35, s33, 31
	s_add_u32 s30, s2, s33
	s_addc_u32 s31, s29, s35
	s_add_u32 s34, s4, s33
	s_addc_u32 s35, s5, s35
	s_add_i32 s2, s19, s27
	s_add_i32 m0, s2, 0x4000
	v_add_u32_e32 v1, s28, v91
	global_load_lds_dwordx4 v84, s[30:31]
	ds_read_b128 v[138:141], v1
	ds_read_b128 v[142:145], v1 offset:1024
	s_add_i32 m0, s2, 0x6000
	ds_read_b128 v[146:149], v1 offset:2048
	global_load_lds_dwordx4 v88, s[30:31]
	ds_read_b128 v[150:153], v1 offset:3072
	ds_read_b128 v[154:157], v1 offset:4096
	s_mov_b32 m0, s2
	ds_read_b128 v[158:161], v1 offset:5120
	global_load_lds_dwordx4 v82, s[34:35]
	ds_read_b128 v[162:165], v1 offset:6144
	ds_read_b128 v[166:169], v1 offset:7168
	s_waitcnt vmcnt(3)
	s_waitcnt lgkmcnt(0)
	s_barrier
	s_setprio 1
	s_waitcnt lgkmcnt(0)
	v_mfma_f32_16x16x32_f16 v[78:81], v[106:109], v[138:141], v[78:81]
	s_add_u32 s30, s30, 0x40000
	s_addc_u32 s31, s31, 0
	s_add_i32 m0, s2, 0x8000
	v_mfma_f32_16x16x32_f16 v[74:77], v[114:117], v[138:141], v[74:77]
	global_load_lds_dwordx4 v84, s[30:31]
	s_add_i32 m0, s2, 0xa000
	v_mfma_f32_16x16x32_f16 v[66:69], v[106:109], v[146:149], v[66:69]
	global_load_lds_dwordx4 v88, s[30:31]
	s_add_i32 m0, s2, 0x2000
	v_mfma_f32_16x16x32_f16 v[58:61], v[114:117], v[146:149], v[58:61]
	global_load_lds_dwordx4 v86, s[34:35]
	v_mfma_f32_16x16x32_f16 v[78:81], v[110:113], v[142:145], v[78:81]
	v_mfma_f32_16x16x32_f16 v[74:77], v[118:121], v[142:145], v[74:77]
	v_mfma_f32_16x16x32_f16 v[66:69], v[110:113], v[150:153], v[66:69]
	v_mfma_f32_16x16x32_f16 v[58:61], v[118:121], v[150:153], v[58:61]
	v_mfma_f32_16x16x32_f16 v[54:57], v[106:109], v[154:157], v[54:57]
	v_mfma_f32_16x16x32_f16 v[46:49], v[114:117], v[154:157], v[46:49]
	v_mfma_f32_16x16x32_f16 v[38:41], v[106:109], v[162:165], v[38:41]
	v_mfma_f32_16x16x32_f16 v[30:33], v[114:117], v[162:165], v[30:33]
	v_mfma_f32_16x16x32_f16 v[54:57], v[110:113], v[158:161], v[54:57]
	v_mfma_f32_16x16x32_f16 v[46:49], v[118:121], v[158:161], v[46:49]
	v_mfma_f32_16x16x32_f16 v[38:41], v[110:113], v[166:169], v[38:41]
	v_mfma_f32_16x16x32_f16 v[30:33], v[118:121], v[166:169], v[30:33]
	v_mfma_f32_16x16x32_f16 v[70:73], v[122:125], v[138:141], v[70:73]
	v_mfma_f32_16x16x32_f16 v[62:65], v[130:133], v[138:141], v[62:65]
	v_mfma_f32_16x16x32_f16 v[50:53], v[122:125], v[146:149], v[50:53]
	v_mfma_f32_16x16x32_f16 v[42:45], v[130:133], v[146:149], v[42:45]
	v_mfma_f32_16x16x32_f16 v[70:73], v[126:129], v[142:145], v[70:73]
	v_mfma_f32_16x16x32_f16 v[62:65], v[134:137], v[142:145], v[62:65]
	v_mfma_f32_16x16x32_f16 v[50:53], v[126:129], v[150:153], v[50:53]
	v_mfma_f32_16x16x32_f16 v[42:45], v[134:137], v[150:153], v[42:45]
	v_mfma_f32_16x16x32_f16 v[34:37], v[122:125], v[154:157], v[34:37]
	v_mfma_f32_16x16x32_f16 v[26:29], v[130:133], v[154:157], v[26:29]
	s_add_i32 s14, s14, 1
	s_bitcmp1_b32 s14, 4
	s_addc_u32 s25, s25, 0
	v_mfma_f32_16x16x32_f16 v[18:21], v[122:125], v[162:165], v[18:21]
	s_and_b32 s14, s14, 15
	v_mfma_f32_16x16x32_f16 v[10:13], v[130:133], v[162:165], v[10:13]
	v_mfma_f32_16x16x32_f16 v[34:37], v[126:129], v[158:161], v[34:37]
	v_mfma_f32_16x16x32_f16 v[26:29], v[134:137], v[158:161], v[26:29]
	s_add_i32 s26, s26, -1
	v_mfma_f32_16x16x32_f16 v[18:21], v[126:129], v[166:169], v[18:21]
	s_mov_b32 s2, s15
	s_mov_b32 s15, s27
	v_mfma_f32_16x16x32_f16 v[10:13], v[134:137], v[166:169], v[10:13]
	s_mov_b32 s27, s28
	s_cmp_lg_u32 s26, 0
	s_setprio 0
	s_barrier
	s_cbranch_scc1 .LBB1_5
	s_ashr_i32 s2, s17, 7
	s_and_b32 s3, s2, -16
	s_or_b32 s2, s3, 2
	s_sub_u32 s14, s10, s8
	s_subb_u32 s11, s11, s9
	s_bfe_u32 s6, s17, 0x50006
	s_add_u32 s14, s8, s14
	s_addc_u32 s15, s9, s11
	s_lshr_b32 s11, s24, 6
	s_or_b32 s17, s11, s3
	s_lshl_b32 s17, s17, 8
	s_lshl_b32 s23, s6, 3
	v_bfe_u32 v93, v105, 3, 3
	v_pk_add_f32 v[80:81], v[24:25], v[80:81]
	v_pk_add_f32 v[78:79], v[22:23], v[78:79]
	v_pk_add_f32 v[74:75], v[14:15], v[74:75]
	s_or_b32 s17, s17, s23
	s_or_b32 s11, s2, s11
	v_cvt_pk_f16_f32 v78, v78, v79
	v_cvt_pk_f16_f32 v79, v80, v81
	v_cvt_pk_f16_f32 v80, v74, v75
	v_or_b32_e32 v74, s17, v93
	s_lshl_b32 s11, s11, 8
	v_ashrrev_i32_e32 v75, 31, v74
	v_pk_add_f32 v[72:73], v[8:9], v[72:73]
	v_pk_add_f32 v[70:71], v[6:7], v[70:71]
	v_pk_add_f32 v[62:63], v[2:3], v[62:63]
	s_or_b32 s11, s11, s23
	v_lshlrev_b64 v[74:75], 10, v[74:75]
	v_cvt_pk_f16_f32 v70, v70, v71
	v_cvt_pk_f16_f32 v71, v72, v73
	v_cvt_pk_f16_f32 v72, v62, v63
	v_or_b32_e32 v62, s11, v93
	v_pk_add_f32 v[76:77], v[16:17], v[76:77]
	v_lshl_add_u64 v[74:75], s[14:15], 0, v[74:75]
	v_ashrrev_i32_e32 v63, 31, v62
	v_cvt_pk_f16_f32 v81, v76, v77
	v_lshl_add_u64 v[76:77], v[74:75], 0, v[98:99]
	v_lshlrev_b64 v[62:63], 10, v[62:63]
	global_store_dwordx4 v[76:77], v[78:81], off
	v_pk_add_f32 v[64:65], v[4:5], v[64:65]
	v_lshl_add_u64 v[76:77], s[14:15], 0, v[62:63]
	v_cvt_pk_f16_f32 v73, v64, v65
	v_lshl_add_u64 v[62:63], v[76:77], 0, v[98:99]
	global_store_dwordx4 v[62:63], v[70:73], off
	v_pk_add_f32 v[64:65], v[24:25], v[68:69]
	v_pk_add_f32 v[62:63], v[22:23], v[66:67]
	v_pk_add_f32 v[60:61], v[16:17], v[60:61]
	v_pk_add_f32 v[58:59], v[14:15], v[58:59]
	v_pk_add_f32 v[52:53], v[8:9], v[52:53]
	v_pk_add_f32 v[50:51], v[6:7], v[50:51]
	v_pk_add_f32 v[44:45], v[4:5], v[44:45]
	v_pk_add_f32 v[42:43], v[2:3], v[42:43]
	v_cvt_pk_f16_f32 v62, v62, v63
	v_cvt_pk_f16_f32 v63, v64, v65
	v_cvt_pk_f16_f32 v64, v58, v59
	v_cvt_pk_f16_f32 v65, v60, v61
	v_lshl_add_u64 v[58:59], v[74:75], 0, v[96:97]
	v_cvt_pk_f16_f32 v50, v50, v51
	v_cvt_pk_f16_f32 v51, v52, v53
	v_cvt_pk_f16_f32 v52, v42, v43
	v_cvt_pk_f16_f32 v53, v44, v45
	v_lshl_add_u64 v[42:43], v[76:77], 0, v[96:97]
	v_mov_b32_e32 v1, 0
	global_store_dwordx4 v[58:59], v[62:65], off
	global_store_dwordx4 v[42:43], v[50:53], off
	v_pk_add_f32 v[44:45], v[24:25], v[56:57]
	v_pk_add_f32 v[42:43], v[22:23], v[54:55]
	v_mov_b32_e32 v95, v1
	v_cvt_pk_f16_f32 v42, v42, v43
	v_cvt_pk_f16_f32 v43, v44, v45
	v_pk_add_f32 v[48:49], v[16:17], v[48:49]
	v_pk_add_f32 v[44:45], v[14:15], v[46:47]
	v_pk_add_f32 v[36:37], v[8:9], v[36:37]
	v_pk_add_f32 v[34:35], v[6:7], v[34:35]
	v_pk_add_f32 v[28:29], v[4:5], v[28:29]
	v_pk_add_f32 v[26:27], v[2:3], v[26:27]
	v_pk_add_f32 v[24:25], v[24:25], v[40:41]
	v_pk_add_f32 v[22:23], v[22:23], v[38:39]
	v_pk_add_f32 v[16:17], v[16:17], v[32:33]
	v_pk_add_f32 v[14:15], v[14:15], v[30:31]
	v_pk_add_f32 v[8:9], v[8:9], v[20:21]
	v_pk_add_f32 v[6:7], v[6:7], v[18:19]
	v_pk_add_f32 v[4:5], v[4:5], v[12:13]
	v_pk_add_f32 v[2:3], v[2:3], v[10:11]
	s_add_u32 s14, s20, s22
	v_cvt_pk_f16_f32 v44, v44, v45
	v_cvt_pk_f16_f32 v45, v48, v49
	v_lshl_add_u64 v[46:47], v[74:75], 0, v[0:1]
	v_cvt_pk_f16_f32 v34, v34, v35
	v_cvt_pk_f16_f32 v35, v36, v37
	v_cvt_pk_f16_f32 v36, v26, v27
	v_cvt_pk_f16_f32 v37, v28, v29
	v_lshl_add_u64 v[26:27], v[76:77], 0, v[0:1]
	v_cvt_pk_f16_f32 v22, v22, v23
	v_cvt_pk_f16_f32 v23, v24, v25
	v_cvt_pk_f16_f32 v24, v14, v15
	v_cvt_pk_f16_f32 v25, v16, v17
	v_lshl_add_u64 v[14:15], v[74:75], 0, v[94:95]
	v_cvt_pk_f16_f32 v6, v6, v7
	v_cvt_pk_f16_f32 v7, v8, v9
	v_cvt_pk_f16_f32 v8, v2, v3
	v_cvt_pk_f16_f32 v9, v4, v5
	v_lshl_add_u64 v[2:3], v[76:77], 0, v[94:95]
	s_addc_u32 s15, s21, 0
	v_mov_b32_e32 v93, v1
	global_store_dwordx4 v[46:47], v[42:45], off
	global_store_dwordx4 v[26:27], v[34:37], off
	global_store_dwordx4 v[14:15], v[22:25], off
	global_store_dwordx4 v[2:3], v[6:9], off
	v_lshl_add_u64 v[2:3], s[14:15], 0, v[92:93]
	s_mov_b64 s[14:15], 0x2000
	v_lshl_add_u64 v[2:3], v[2:3], 0, s[14:15]
	global_load_dwordx4 v[20:23], v[2:3], off
	global_load_dwordx4 v[12:15], v[2:3], off offset:16
	global_load_dwordx4 v[8:11], v[2:3], off offset:512
	global_load_dwordx4 v[4:7], v[2:3], off offset:528
	s_add_u32 s11, s12, 0x400000
	s_mov_b32 s7, 2
	v_and_b32_e32 v106, 56, v105
	s_mov_b32 s10, 0
	s_addc_u32 s12, s13, 0
	s_mov_b32 s14, 0xc000
	s_mov_b32 s17, 0x18000
	s_mov_b32 s13, 16
	v_mov_b32_e32 v0, v1
	v_mov_b32_e32 v2, v1
	v_mov_b32_e32 v3, v1
	v_mov_b32_e32 v16, v1
	v_mov_b32_e32 v17, v1
	v_mov_b32_e32 v18, v1
	v_mov_b32_e32 v19, v1
	v_mov_b32_e32 v24, v1
	v_mov_b32_e32 v25, v1
	v_mov_b32_e32 v26, v1
	v_mov_b32_e32 v27, v1
	v_mov_b32_e32 v32, v1
	v_mov_b32_e32 v33, v1
	v_mov_b32_e32 v34, v1
	v_mov_b32_e32 v35, v1
	v_mov_b32_e32 v40, v1
	v_mov_b32_e32 v41, v1
	v_mov_b32_e32 v42, v1
	v_mov_b32_e32 v43, v1
	v_mov_b32_e32 v48, v1
	v_mov_b32_e32 v49, v1
	v_mov_b32_e32 v50, v1
	v_mov_b32_e32 v51, v1
	v_mov_b32_e32 v60, v1
	v_mov_b32_e32 v61, v1
	v_mov_b32_e32 v62, v1
	v_mov_b32_e32 v63, v1
	v_mov_b32_e32 v68, v1
	v_mov_b32_e32 v69, v1
	v_mov_b32_e32 v70, v1
	v_mov_b32_e32 v71, v1
	v_mov_b32_e32 v28, v1
	v_mov_b32_e32 v29, v1
	v_mov_b32_e32 v30, v1
	v_mov_b32_e32 v31, v1
	v_mov_b32_e32 v36, v1
	v_mov_b32_e32 v37, v1
	v_mov_b32_e32 v38, v1
	v_mov_b32_e32 v39, v1
	v_mov_b32_e32 v44, v1
	v_mov_b32_e32 v45, v1
	v_mov_b32_e32 v46, v1
	v_mov_b32_e32 v47, v1
	v_mov_b32_e32 v52, v1
	v_mov_b32_e32 v53, v1
	v_mov_b32_e32 v54, v1
	v_mov_b32_e32 v55, v1
	v_mov_b32_e32 v56, v1
	v_mov_b32_e32 v57, v1
	v_mov_b32_e32 v58, v1
	v_mov_b32_e32 v59, v1
	v_mov_b32_e32 v64, v1
	v_mov_b32_e32 v65, v1
	v_mov_b32_e32 v66, v1
	v_mov_b32_e32 v67, v1
	v_mov_b32_e32 v72, v1
	v_mov_b32_e32 v73, v1
	v_mov_b32_e32 v74, v1
	v_mov_b32_e32 v75, v1
	v_mov_b32_e32 v76, v1
	v_mov_b32_e32 v77, v1
	v_mov_b32_e32 v78, v1
	v_mov_b32_e32 v79, v1
.LBB1_7:
	s_mov_b32 s15, s17
	v_add_u32_e32 v80, s15, v101
	ds_read_b128 v[92:95], v80 offset:16384
	ds_read_b128 v[96:99], v80 offset:17408
	ds_read_b128 v[108:111], v80 offset:18432
	ds_read_b128 v[112:115], v80 offset:19456
	ds_read_b128 v[116:119], v80 offset:32768
	ds_read_b128 v[120:123], v80 offset:33792
	ds_read_b128 v[124:127], v80 offset:34816
	ds_read_b128 v[128:131], v80 offset:35840
	s_lshl_b32 s17, s7, 7
	s_ashr_i32 s23, s17, 31
	s_add_u32 s20, s11, s17
	s_addc_u32 s21, s12, s23
	s_add_u32 s22, s4, s17
	s_addc_u32 s23, s5, s23
	s_add_i32 s17, s19, s14
	s_add_i32 m0, s17, 0x4000
	v_add_u32_e32 v80, s15, v91
	global_load_lds_dwordx4 v84, s[20:21]
	ds_read_b128 v[132:135], v80
	ds_read_b128 v[136:139], v80 offset:1024
	s_add_i32 m0, s17, 0x6000
	ds_read_b128 v[140:143], v80 offset:2048
	global_load_lds_dwordx4 v88, s[20:21]
	ds_read_b128 v[144:147], v80 offset:3072
	ds_read_b128 v[148:151], v80 offset:4096
	s_mov_b32 m0, s17
	ds_read_b128 v[152:155], v80 offset:5120
	global_load_lds_dwordx4 v82, s[22:23]
	ds_read_b128 v[156:159], v80 offset:6144
	ds_read_b128 v[160:163], v80 offset:7168
	s_waitcnt vmcnt(3)
	s_waitcnt lgkmcnt(0)
	s_barrier
	s_setprio 1
	s_waitcnt lgkmcnt(0)
	v_mfma_f32_16x16x32_f16 v[76:79], v[92:95], v[132:135], v[76:79]
	s_add_u32 s20, s20, 0x40000
	s_addc_u32 s21, s21, 0
	s_add_i32 m0, s17, 0x8000
	v_mfma_f32_16x16x32_f16 v[72:75], v[108:111], v[132:135], v[72:75]
	global_load_lds_dwordx4 v84, s[20:21]
	s_add_i32 m0, s17, 0xa000
	v_mfma_f32_16x16x32_f16 v[64:67], v[92:95], v[140:143], v[64:67]
	global_load_lds_dwordx4 v88, s[20:21]
	s_add_i32 m0, s17, 0x2000
	v_mfma_f32_16x16x32_f16 v[56:59], v[108:111], v[140:143], v[56:59]
	global_load_lds_dwordx4 v86, s[22:23]
	v_mfma_f32_16x16x32_f16 v[76:79], v[96:99], v[136:139], v[76:79]
	v_mfma_f32_16x16x32_f16 v[72:75], v[112:115], v[136:139], v[72:75]
	v_mfma_f32_16x16x32_f16 v[64:67], v[96:99], v[144:147], v[64:67]
	v_mfma_f32_16x16x32_f16 v[56:59], v[112:115], v[144:147], v[56:59]
	v_mfma_f32_16x16x32_f16 v[52:55], v[92:95], v[148:151], v[52:55]
	v_mfma_f32_16x16x32_f16 v[44:47], v[108:111], v[148:151], v[44:47]
	v_mfma_f32_16x16x32_f16 v[36:39], v[92:95], v[156:159], v[36:39]
	v_mfma_f32_16x16x32_f16 v[28:31], v[108:111], v[156:159], v[28:31]
	v_mfma_f32_16x16x32_f16 v[52:55], v[96:99], v[152:155], v[52:55]
	v_mfma_f32_16x16x32_f16 v[44:47], v[112:115], v[152:155], v[44:47]
	v_mfma_f32_16x16x32_f16 v[36:39], v[96:99], v[160:163], v[36:39]
	v_mfma_f32_16x16x32_f16 v[28:31], v[112:115], v[160:163], v[28:31]
	v_mfma_f32_16x16x32_f16 v[68:71], v[116:119], v[132:135], v[68:71]
	v_mfma_f32_16x16x32_f16 v[60:63], v[124:127], v[132:135], v[60:63]
	v_mfma_f32_16x16x32_f16 v[48:51], v[116:119], v[140:143], v[48:51]
	v_mfma_f32_16x16x32_f16 v[40:43], v[124:127], v[140:143], v[40:43]
	v_mfma_f32_16x16x32_f16 v[68:71], v[120:123], v[136:139], v[68:71]
	v_mfma_f32_16x16x32_f16 v[60:63], v[128:131], v[136:139], v[60:63]
	v_mfma_f32_16x16x32_f16 v[48:51], v[120:123], v[144:147], v[48:51]
	v_mfma_f32_16x16x32_f16 v[40:43], v[128:131], v[144:147], v[40:43]
	v_mfma_f32_16x16x32_f16 v[32:35], v[116:119], v[148:151], v[32:35]
	v_mfma_f32_16x16x32_f16 v[24:27], v[124:127], v[148:151], v[24:27]
	s_add_i32 s7, s7, 1
	s_cmp_lg_u32 s7, 16
	v_mfma_f32_16x16x32_f16 v[16:19], v[116:119], v[156:159], v[16:19]
	s_cselect_b32 s7, s7, 0
	v_mfma_f32_16x16x32_f16 v[0:3], v[124:127], v[156:159], v[0:3]
	s_add_i32 s13, s13, -1
	v_mfma_f32_16x16x32_f16 v[32:35], v[120:123], v[152:155], v[32:35]
	s_mov_b32 s17, s10
	v_mfma_f32_16x16x32_f16 v[24:27], v[128:131], v[152:155], v[24:27]
	s_mov_b32 s10, s14
	v_mfma_f32_16x16x32_f16 v[16:19], v[120:123], v[160:163], v[16:19]
	s_mov_b32 s14, s15
	v_mfma_f32_16x16x32_f16 v[0:3], v[128:131], v[160:163], v[0:3]
	s_cmp_lg_u32 s13, 0
	s_setprio 0
	s_barrier
	s_cbranch_scc1 .LBB1_7
	s_sub_u32 s0, s0, s8
	s_subb_u32 s1, s1, s9
	s_add_u32 s0, s8, s0
	s_addc_u32 s1, s9, s1
	s_lshl_b32 s3, s3, 6
	s_or_b32 s3, s3, s16
	s_lshl_b32 s4, s6, 1
	v_lshrrev_b32_e32 v86, 5, v106
	v_pk_add_f32 v[78:79], v[22:23], v[78:79]
	v_pk_add_f32 v[76:77], v[20:21], v[76:77]
	v_pk_add_f32 v[72:73], v[12:13], v[72:73]
	s_or_b32 s3, s3, s4
	s_lshl_b32 s2, s2, 6
	v_cvt_pk_f16_f32 v76, v76, v77
	v_cvt_pk_f16_f32 v77, v78, v79
	v_cvt_pk_f16_f32 v78, v72, v73
	v_or_b32_e32 v72, s3, v86
	s_or_b32 s2, s2, s16
	v_ashrrev_i32_e32 v73, 31, v72
	v_pk_add_f32 v[70:71], v[10:11], v[70:71]
	v_pk_add_f32 v[68:69], v[8:9], v[68:69]
	v_pk_add_f32 v[60:61], v[4:5], v[60:61]
	s_or_b32 s2, s2, s4
	v_lshlrev_b64 v[72:73], 12, v[72:73]
	v_cvt_pk_f16_f32 v68, v68, v69
	v_cvt_pk_f16_f32 v69, v70, v71
	v_cvt_pk_f16_f32 v70, v60, v61
	v_or_b32_e32 v60, s2, v86
	v_mov_b32_e32 v91, 0
	v_pk_add_f32 v[74:75], v[14:15], v[74:75]
	v_lshl_add_u64 v[72:73], s[0:1], 0, v[72:73]
	v_ashrrev_i32_e32 v61, 31, v60
	v_cvt_pk_f16_f32 v79, v74, v75
	v_lshl_add_u64 v[74:75], v[72:73], 0, v[90:91]
	v_lshlrev_b64 v[60:61], 12, v[60:61]
	v_lshl_or_b32 v84, v102, 6, v100
	v_mov_b32_e32 v85, v91
	global_store_dwordx4 v[74:75], v[76:79], off sc1
	v_lshl_add_u64 v[74:75], s[0:1], 0, v[60:61]
	v_pk_add_f32 v[50:51], v[10:11], v[50:51]
	v_pk_add_f32 v[48:49], v[8:9], v[48:49]
	v_pk_add_f32 v[42:43], v[6:7], v[42:43]
	v_pk_add_f32 v[40:41], v[4:5], v[40:41]
	v_pk_add_f32 v[62:63], v[6:7], v[62:63]
	v_cvt_pk_f16_f32 v48, v48, v49
	v_cvt_pk_f16_f32 v49, v50, v51
	v_cvt_pk_f16_f32 v50, v40, v41
	v_cvt_pk_f16_f32 v51, v42, v43
	v_lshl_add_u64 v[40:41], v[74:75], 0, v[84:85]
	v_cvt_pk_f16_f32 v71, v62, v63
	v_lshl_add_u64 v[60:61], v[74:75], 0, v[90:91]
	global_store_dwordx4 v[40:41], v[48:51], off sc1
	v_pk_add_f32 v[42:43], v[22:23], v[54:55]
	v_pk_add_f32 v[40:41], v[20:21], v[52:53]
	v_lshl_or_b32 v80, v103, 6, v100
	v_lshl_or_b32 v82, v104, 6, v100
	v_mov_b32_e32 v81, v91
	v_mov_b32_e32 v83, v91
	global_store_dwordx4 v[60:61], v[68:71], off sc1
	v_pk_add_f32 v[62:63], v[22:23], v[66:67]
	v_pk_add_f32 v[60:61], v[20:21], v[64:65]
	v_pk_add_f32 v[58:59], v[14:15], v[58:59]
	v_pk_add_f32 v[56:57], v[12:13], v[56:57]
	v_cvt_pk_f16_f32 v40, v40, v41
	v_cvt_pk_f16_f32 v41, v42, v43
	v_pk_add_f32 v[46:47], v[14:15], v[46:47]
	v_pk_add_f32 v[42:43], v[12:13], v[44:45]
	v_pk_add_f32 v[34:35], v[10:11], v[34:35]
	v_pk_add_f32 v[32:33], v[8:9], v[32:33]
	v_pk_add_f32 v[26:27], v[6:7], v[26:27]
	v_pk_add_f32 v[24:25], v[4:5], v[24:25]
	v_pk_add_f32 v[22:23], v[22:23], v[38:39]
	v_pk_add_f32 v[20:21], v[20:21], v[36:37]
	v_pk_add_f32 v[14:15], v[14:15], v[30:31]
	v_pk_add_f32 v[12:13], v[12:13], v[28:29]
	v_pk_add_f32 v[10:11], v[10:11], v[18:19]
	v_pk_add_f32 v[8:9], v[8:9], v[16:17]
	v_pk_add_f32 v[2:3], v[6:7], v[2:3]
	v_pk_add_f32 v[0:1], v[4:5], v[0:1]
	v_cvt_pk_f16_f32 v60, v60, v61
	v_cvt_pk_f16_f32 v61, v62, v63
	v_cvt_pk_f16_f32 v62, v56, v57
	v_cvt_pk_f16_f32 v63, v58, v59
	v_lshl_add_u64 v[56:57], v[72:73], 0, v[84:85]
	v_cvt_pk_f16_f32 v42, v42, v43
	v_cvt_pk_f16_f32 v43, v46, v47
	v_lshl_add_u64 v[44:45], v[72:73], 0, v[80:81]
	v_cvt_pk_f16_f32 v32, v32, v33
	v_cvt_pk_f16_f32 v33, v34, v35
	v_cvt_pk_f16_f32 v34, v24, v25
	v_cvt_pk_f16_f32 v35, v26, v27
	v_lshl_add_u64 v[24:25], v[74:75], 0, v[80:81]
	v_cvt_pk_f16_f32 v20, v20, v21
	v_cvt_pk_f16_f32 v21, v22, v23
	v_cvt_pk_f16_f32 v22, v12, v13
	v_cvt_pk_f16_f32 v23, v14, v15
	v_lshl_add_u64 v[12:13], v[72:73], 0, v[82:83]
	v_cvt_pk_f16_f32 v8, v8, v9
	v_cvt_pk_f16_f32 v9, v10, v11
	v_cvt_pk_f16_f32 v10, v0, v1
	v_cvt_pk_f16_f32 v11, v2, v3
	v_lshl_add_u64 v[0:1], v[74:75], 0, v[82:83]
	global_store_dwordx4 v[56:57], v[60:63], off sc1
	global_store_dwordx4 v[44:45], v[40:43], off sc1
	global_store_dwordx4 v[24:25], v[32:35], off sc1
	global_store_dwordx4 v[12:13], v[20:23], off sc1
	global_store_dwordx4 v[0:1], v[8:11], off sc1
	s_waitcnt vmcnt(0)
	s_cmpk_gt_u32 s18, 0xff
	s_cbranch_scc1 .LBB1_10
	s_barrier

.LBB2_3:
	s_mov_b32 s16, s15
	v_add_u32_e32 v116, s16, v87
	v_add_u32_e32 v148, s16, v0
	ds_read_b128 v[88:91], v116 offset:16384
	ds_read_b128 v[92:95], v116 offset:17408
	ds_read_b128 v[96:99], v116 offset:18432
	ds_read_b128 v[100:103], v116 offset:19456
	ds_read_b128 v[104:107], v116 offset:32768
	ds_read_b128 v[108:111], v116 offset:33792
	ds_read_b128 v[112:115], v116 offset:34816
	ds_read_b128 v[116:119], v116 offset:35840
	s_lshl_b32 s15, s7, 7
	s_ashr_i32 s17, s15, 31
	s_add_u32 s18, s4, s15
	s_addc_u32 s19, s5, s17
	s_add_u32 s20, s2, s15
	s_addc_u32 s21, s3, s17
	s_add_i32 s15, s6, s14
	s_add_i32 m0, s15, 0x4000
	ds_read_b128 v[120:123], v148
	global_load_lds_dwordx4 v82, s[18:19]
	ds_read_b128 v[124:127], v148 offset:1024
	s_add_i32 m0, s15, 0x6000
	ds_read_b128 v[128:131], v148 offset:2048
	global_load_lds_dwordx4 v84, s[18:19]
	ds_read_b128 v[132:135], v148 offset:3072
	ds_read_b128 v[136:139], v148 offset:4096
	s_mov_b32 m0, s15
	ds_read_b128 v[140:143], v148 offset:5120
	global_load_lds_dwordx4 v82, s[20:21]
	ds_read_b128 v[144:147], v148 offset:6144
	ds_read_b128 v[148:151], v148 offset:7168
	s_waitcnt vmcnt(3)
	s_waitcnt lgkmcnt(0)
	s_barrier
	s_setprio 1
	s_waitcnt lgkmcnt(0)
	v_mfma_f32_16x16x32_f16 v[18:21], v[88:91], v[120:123], v[18:21]
	s_add_u32 s18, s18, 0x40000
	s_addc_u32 s19, s19, 0
	s_add_i32 m0, s15, 0x8000
	v_mfma_f32_16x16x32_f16 v[70:73], v[96:99], v[120:123], v[70:73]
	global_load_lds_dwordx4 v82, s[18:19]
	s_add_i32 m0, s15, 0xa000
	v_mfma_f32_16x16x32_f16 v[58:61], v[88:91], v[128:131], v[58:61]
	global_load_lds_dwordx4 v84, s[18:19]
	s_add_i32 m0, s15, 0x2000
	v_mfma_f32_16x16x32_f16 v[54:57], v[96:99], v[128:131], v[54:57]
	global_load_lds_dwordx4 v84, s[20:21]
	v_mfma_f32_16x16x32_f16 v[18:21], v[92:95], v[124:127], v[18:21]
	v_mfma_f32_16x16x32_f16 v[70:73], v[100:103], v[124:127], v[70:73]
	v_mfma_f32_16x16x32_f16 v[58:61], v[92:95], v[132:135], v[58:61]
	v_mfma_f32_16x16x32_f16 v[54:57], v[100:103], v[132:135], v[54:57]
	v_mfma_f32_16x16x32_f16 v[42:45], v[88:91], v[136:139], v[42:45]
	v_mfma_f32_16x16x32_f16 v[38:41], v[96:99], v[136:139], v[38:41]
	v_mfma_f32_16x16x32_f16 v[26:29], v[88:91], v[144:147], v[26:29]
	v_mfma_f32_16x16x32_f16 v[22:25], v[96:99], v[144:147], v[22:25]
	v_mfma_f32_16x16x32_f16 v[42:45], v[92:95], v[140:143], v[42:45]
	v_mfma_f32_16x16x32_f16 v[38:41], v[100:103], v[140:143], v[38:41]
	v_mfma_f32_16x16x32_f16 v[26:29], v[92:95], v[148:151], v[26:29]
	v_mfma_f32_16x16x32_f16 v[22:25], v[100:103], v[148:151], v[22:25]
	v_mfma_f32_16x16x32_f16 v[78:81], v[104:107], v[120:123], v[78:81]
	v_mfma_f32_16x16x32_f16 v[74:77], v[112:115], v[120:123], v[74:77]
	v_mfma_f32_16x16x32_f16 v[66:69], v[104:107], v[128:131], v[66:69]
	v_mfma_f32_16x16x32_f16 v[62:65], v[112:115], v[128:131], v[62:65]
	v_mfma_f32_16x16x32_f16 v[78:81], v[108:111], v[124:127], v[78:81]
	v_mfma_f32_16x16x32_f16 v[74:77], v[116:119], v[124:127], v[74:77]
	v_mfma_f32_16x16x32_f16 v[66:69], v[108:111], v[132:135], v[66:69]
	v_mfma_f32_16x16x32_f16 v[62:65], v[116:119], v[132:135], v[62:65]
	v_mfma_f32_16x16x32_f16 v[50:53], v[104:107], v[136:139], v[50:53]
	v_mfma_f32_16x16x32_f16 v[46:49], v[112:115], v[136:139], v[46:49]
	s_add_i32 s7, s7, 1
	s_cmp_lg_u32 s7, 16
	v_mfma_f32_16x16x32_f16 v[34:37], v[104:107], v[144:147], v[34:37]
	s_cselect_b32 s7, s7, 0
	v_mfma_f32_16x16x32_f16 v[30:33], v[112:115], v[144:147], v[30:33]
	s_add_i32 s11, s11, -1
	v_mfma_f32_16x16x32_f16 v[50:53], v[108:111], v[140:143], v[50:53]
	s_mov_b32 s15, s13
	v_mfma_f32_16x16x32_f16 v[46:49], v[116:119], v[140:143], v[46:49]
	s_mov_b32 s13, s14
	v_mfma_f32_16x16x32_f16 v[34:37], v[108:111], v[148:151], v[34:37]
	s_mov_b32 s14, s16
	v_mfma_f32_16x16x32_f16 v[30:33], v[116:119], v[148:151], v[30:33]
	s_cmp_lg_u32 s11, 0
	s_setprio 0
	s_barrier
	s_cbranch_scc1 .LBB2_3
	v_lshl_add_u32 v0, s0, 7, v86
	v_or_b32_e32 v88, s10, v1
	v_ashrrev_i32_e32 v1, 31, v0
	v_lshlrev_b64 v[82:83], 12, v[0:1]
	v_or_b32_e32 v88, s1, v88
	v_lshl_add_u64 v[82:83], s[8:9], 0, v[82:83]
	v_lshlrev_b32_e32 v88, 2, v88
	v_mov_b32_e32 v89, 0
	v_or_b32_e32 v84, 16, v0
	v_lshl_add_u64 v[82:83], v[82:83], 0, v[88:89]
	v_pk_add_f32 v[20:21], v[16:17], v[20:21]
	v_pk_add_f32 v[18:19], v[14:15], v[18:19]
	v_ashrrev_i32_e32 v85, 31, v84
	global_store_dwordx4 v[82:83], v[18:21], off sc1
	v_lshlrev_b64 v[84:85], 12, v[84:85]
	v_lshl_add_u64 v[84:85], s[8:9], 0, v[84:85]
	v_pk_add_f32 v[20:21], v[12:13], v[72:73]
	v_pk_add_f32 v[18:19], v[10:11], v[70:71]
	global_store_dwordx4 v[82:83], v[18:21], off offset:64 sc1
	v_or_b32_e32 v86, 32, v0
	v_lshl_add_u64 v[84:85], v[84:85], 0, v[88:89]
	v_pk_add_f32 v[20:21], v[8:9], v[80:81]
	v_pk_add_f32 v[18:19], v[6:7], v[78:79]
	global_store_dwordx4 v[82:83], v[18:21], off offset:512 sc1
	v_ashrrev_i32_e32 v87, 31, v86
	v_lshlrev_b64 v[86:87], 12, v[86:87]
	v_pk_add_f32 v[20:21], v[4:5], v[76:77]
	v_pk_add_f32 v[18:19], v[2:3], v[74:75]
	global_store_dwordx4 v[82:83], v[18:21], off offset:576 sc1
	v_lshl_add_u64 v[86:87], s[8:9], 0, v[86:87]
	v_or_b32_e32 v0, 48, v0
	v_pk_add_f32 v[20:21], v[16:17], v[60:61]
	v_pk_add_f32 v[18:19], v[14:15], v[58:59]
	global_store_dwordx4 v[84:85], v[18:21], off sc1
	v_ashrrev_i32_e32 v1, 31, v0
	v_lshl_add_u64 v[86:87], v[86:87], 0, v[88:89]
	v_pk_add_f32 v[20:21], v[12:13], v[56:57]
	v_pk_add_f32 v[18:19], v[10:11], v[54:55]
	global_store_dwordx4 v[84:85], v[18:21], off offset:64 sc1
	v_lshlrev_b64 v[0:1], 12, v[0:1]
	v_lshl_add_u64 v[0:1], s[8:9], 0, v[0:1]
	v_pk_add_f32 v[20:21], v[8:9], v[68:69]
	v_pk_add_f32 v[18:19], v[6:7], v[66:67]
	global_store_dwordx4 v[84:85], v[18:21], off offset:512 sc1
	v_lshl_add_u64 v[0:1], v[0:1], 0, v[88:89]
	s_cmpk_gt_u32 s12, 0xff
	v_pk_add_f32 v[20:21], v[4:5], v[64:65]
	v_pk_add_f32 v[18:19], v[2:3], v[62:63]
	global_store_dwordx4 v[84:85], v[18:21], off offset:576 sc1
	s_nop 1
	v_pk_add_f32 v[20:21], v[16:17], v[44:45]
	v_pk_add_f32 v[18:19], v[14:15], v[42:43]
	global_store_dwordx4 v[86:87], v[18:21], off sc1
	v_pk_add_f32 v[16:17], v[16:17], v[28:29]
	v_pk_add_f32 v[14:15], v[14:15], v[26:27]
	v_pk_add_f32 v[20:21], v[12:13], v[40:41]
	v_pk_add_f32 v[18:19], v[10:11], v[38:39]
	global_store_dwordx4 v[86:87], v[18:21], off offset:64 sc1
	v_pk_add_f32 v[12:13], v[12:13], v[24:25]
	v_pk_add_f32 v[10:11], v[10:11], v[22:23]
	v_pk_add_f32 v[20:21], v[8:9], v[52:53]
	v_pk_add_f32 v[18:19], v[6:7], v[50:51]
	global_store_dwordx4 v[86:87], v[18:21], off offset:512 sc1
	v_pk_add_f32 v[8:9], v[8:9], v[36:37]
	v_pk_add_f32 v[6:7], v[6:7], v[34:35]
	v_pk_add_f32 v[20:21], v[4:5], v[48:49]
	v_pk_add_f32 v[18:19], v[2:3], v[46:47]
	v_pk_add_f32 v[4:5], v[4:5], v[32:33]
	v_pk_add_f32 v[2:3], v[2:3], v[30:31]
	global_store_dwordx4 v[86:87], v[18:21], off offset:576 sc1
	global_store_dwordx4 v[0:1], v[14:17], off sc1
	global_store_dwordx4 v[0:1], v[10:13], off offset:64 sc1
	global_store_dwordx4 v[0:1], v[6:9], off offset:512 sc1
	global_store_dwordx4 v[0:1], v[2:5], off offset:576 sc1
	s_waitcnt vmcnt(0)
	s_cbranch_scc1 .LBB2_6
	s_barrier
